# p7 router softmax: 16-lane max and sum via DPP instead of eight dependent ds_bpermute round trips per pass
# speedup vs baseline: 1.0056x; 1.0052x over previous
; #define LAS __attribute__((address_space(3)))
; __device__ __forceinline__ unsigned pk2(float lo, float hi) { f32x2_t v = {lo, hi}; bf16x2_t b = __builtin_convertvector(v, bf16x2_t); return __builtin_bit_cast(unsigned, b); }
; __device__ __forceinline__ float bflo(unsigned w) { return __uint_as_float(w << 16); }
; __device__ __forceinline__ float bfhi(unsigned w) { return __uint_as_float(w & 0xffff0000u); }
; __device__ __forceinline__ void lds_barrier() { asm volatile("s_waitcnt lgkmcnt(0)" ::: "memory"); __builtin_amdgcn_s_barrier(); asm volatile("" ::: "memory"); }
; __device__ __forceinline__ void thin_stage_row(LAS unsigned char* L, int srow, const f32x4 (&h)[4], int lane) {
; #pragma unroll
;     for (int j = 0; j < 4; ++j) { const int k = 4 * (lane + 64 * j);
;         const u32x2 hi = {pk2(h[j][0], h[j][1]), pk2(h[j][2], h[j][3])};
;         const u32x2 lo = {pk2(h[j][0] - bflo(hi.x), h[j][1] - bfhi(hi.x)), pk2(h[j][2] - bflo(hi.y), h[j][3] - bfhi(hi.y))};
;         *(LAS u32x2*)(L + TH_HHI + srow * TH_STR + k * 2) = hi; *(LAS u32x2*)(L + TH_HLO + srow * TH_STR + k * 2) = lo; }
; }
; __device__ __forceinline__ void p7_norm2(const Frame& F, int layer) {
;     ...
;         thin_stage_row(F.lds, 2 * F.wave, va, lane); thin_stage_row(F.lds, 2 * F.wave + 1, vb, lane);
;         lds_barrier();
.LBB0_837:
	v_cvt_pk_bf16_f32 v108, v82, v83
	v_cvt_pk_bf16_f32 v109, v78, v79
	v_lshlrev_b32_e32 v110, 16, v108
	v_and_b32_e32 v111, 0xffff0000, v108
	v_pk_add_f32 v[82:83], v[82:83], v[110:111] neg_lo:[0,1] neg_hi:[0,1]
	v_lshlrev_b32_e32 v110, 16, v109
	v_and_b32_e32 v111, 0xffff0000, v109
	v_pk_add_f32 v[78:79], v[78:79], v[110:111] neg_lo:[0,1] neg_hi:[0,1]
	v_cvt_pk_bf16_f32 v82, v82, v83
	v_cvt_pk_bf16_f32 v83, v78, v79
	v_cvt_pk_bf16_f32 v78, v86, v87
	v_cvt_pk_bf16_f32 v79, v80, v81
	v_lshlrev_b32_e32 v110, 16, v78
	v_and_b32_e32 v111, 0xffff0000, v78
	v_pk_add_f32 v[86:87], v[86:87], v[110:111] neg_lo:[0,1] neg_hi:[0,1]
	v_lshlrev_b32_e32 v110, 16, v79
	v_and_b32_e32 v111, 0xffff0000, v79
	v_add_u32_e32 v107, s29, v94
	v_pk_add_f32 v[80:81], v[80:81], v[110:111] neg_lo:[0,1] neg_hi:[0,1]
	v_add_u32_e32 v112, s30, v94
	v_cvt_pk_bf16_f32 v86, v86, v87
	v_cvt_pk_bf16_f32 v87, v80, v81
	ds_write2st64_b64 v107, v[108:109], v[78:79] offset1:1
	ds_write2st64_b64 v112, v[82:83], v[86:87] offset1:1
	v_cvt_pk_bf16_f32 v78, v90, v91
	v_cvt_pk_bf16_f32 v79, v84, v85
	v_lshlrev_b32_e32 v80, 16, v78
	v_and_b32_e32 v81, 0xffff0000, v78
	v_lshlrev_b32_e32 v82, 16, v79
	v_and_b32_e32 v83, 0xffff0000, v79
	v_pk_add_f32 v[80:81], v[90:91], v[80:81] neg_lo:[0,1] neg_hi:[0,1]
	v_pk_add_f32 v[82:83], v[84:85], v[82:83] neg_lo:[0,1] neg_hi:[0,1]
	v_cvt_pk_bf16_f32 v80, v80, v81
	v_cvt_pk_bf16_f32 v81, v82, v83
	v_cvt_pk_bf16_f32 v82, v92, v93
	v_cvt_pk_bf16_f32 v83, v88, v89
	v_lshlrev_b32_e32 v84, 16, v82
	v_and_b32_e32 v85, 0xffff0000, v82
	v_lshlrev_b32_e32 v86, 16, v83
	v_and_b32_e32 v87, 0xffff0000, v83
	v_pk_add_f32 v[84:85], v[92:93], v[84:85] neg_lo:[0,1] neg_hi:[0,1]
	v_pk_add_f32 v[86:87], v[88:89], v[86:87] neg_lo:[0,1] neg_hi:[0,1]
	v_cvt_pk_bf16_f32 v84, v84, v85
	v_cvt_pk_bf16_f32 v85, v86, v87
	ds_write2st64_b64 v107, v[78:79], v[82:83] offset0:2 offset1:3
	ds_write2st64_b64 v112, v[80:81], v[84:85] offset0:2 offset1:3
	v_cvt_pk_bf16_f32 v78, v66, v67
	v_cvt_pk_bf16_f32 v79, v62, v63
	v_lshlrev_b32_e32 v80, 16, v78
	v_and_b32_e32 v81, 0xffff0000, v78
	v_pk_add_f32 v[66:67], v[66:67], v[80:81] neg_lo:[0,1] neg_hi:[0,1]
	v_lshlrev_b32_e32 v80, 16, v79
	v_and_b32_e32 v81, 0xffff0000, v79
	v_pk_add_f32 v[62:63], v[62:63], v[80:81] neg_lo:[0,1] neg_hi:[0,1]
	v_cvt_pk_bf16_f32 v66, v66, v67
	v_cvt_pk_bf16_f32 v67, v62, v63
	v_cvt_pk_bf16_f32 v62, v70, v71
	ds_write_b64 v103, v[78:79]
	ds_write_b64 v104, v[66:67]
	v_cvt_pk_bf16_f32 v63, v64, v65
	v_lshlrev_b32_e32 v66, 16, v62
	v_and_b32_e32 v67, 0xffff0000, v62
	v_pk_add_f32 v[66:67], v[70:71], v[66:67] neg_lo:[0,1] neg_hi:[0,1]
	v_lshlrev_b32_e32 v70, 16, v63
	v_and_b32_e32 v71, 0xffff0000, v63
	v_pk_add_f32 v[64:65], v[64:65], v[70:71] neg_lo:[0,1] neg_hi:[0,1]
	v_cvt_pk_bf16_f32 v66, v66, v67
	v_cvt_pk_bf16_f32 v67, v64, v65
	v_cvt_pk_bf16_f32 v64, v74, v75
	v_cvt_pk_bf16_f32 v65, v68, v69
	v_lshlrev_b32_e32 v70, 16, v64
	v_and_b32_e32 v71, 0xffff0000, v64
	v_pk_add_f32 v[70:71], v[74:75], v[70:71] neg_lo:[0,1] neg_hi:[0,1]
	v_lshlrev_b32_e32 v74, 16, v65
	v_and_b32_e32 v75, 0xffff0000, v65
	v_add_u32_e32 v78, s34, v94
	v_pk_add_f32 v[68:69], v[68:69], v[74:75] neg_lo:[0,1] neg_hi:[0,1]
	v_add_u32_e32 v79, s35, v94
	v_cvt_pk_bf16_f32 v70, v70, v71
	v_cvt_pk_bf16_f32 v71, v68, v69
	ds_write2st64_b64 v78, v[62:63], v[64:65] offset0:1 offset1:2
	ds_write2st64_b64 v79, v[66:67], v[70:71] offset0:1 offset1:2
	v_cvt_pk_bf16_f32 v62, v76, v77
	v_cvt_pk_bf16_f32 v63, v72, v73
	v_lshlrev_b32_e32 v64, 16, v62
	v_and_b32_e32 v65, 0xffff0000, v62
	v_lshlrev_b32_e32 v66, 16, v63
	v_and_b32_e32 v67, 0xffff0000, v63
	v_pk_add_f32 v[64:65], v[76:77], v[64:65] neg_lo:[0,1] neg_hi:[0,1]
	v_pk_add_f32 v[66:67], v[72:73], v[66:67] neg_lo:[0,1] neg_hi:[0,1]
	v_cvt_pk_bf16_f32 v64, v64, v65
	v_cvt_pk_bf16_f32 v65, v66, v67
	ds_write_b64 v78, v[62:63] offset:1536
	ds_write_b64 v79, v[64:65] offset:1536
	s_waitcnt lgkmcnt(0)
	s_barrier
; #define LAS __attribute__((address_space(3)))
; __device__ __forceinline__ float shx(float v, int m, int lane) { return __int_as_float(__builtin_amdgcn_ds_bpermute((lane ^ m) << 2, __float_as_int(v))); }
; __device__ __forceinline__ void lds_barrier() { asm volatile("s_waitcnt lgkmcnt(0)" ::: "memory"); __builtin_amdgcn_s_barrier(); asm volatile("" ::: "memory"); }
; __device__ __forceinline__ void thin_mfma_partial(LAS unsigned char* L, int wave, int lane) {
;     const int fr = lane & 15, fq = lane >> 4;
;     f32x4 acc = {0.f, 0.f, 0.f, 0.f};
; #pragma unroll
;     for (int s = 0; s < 4; ++s) { const int off = fr * TH_STR + (32 * (4 * wave + s) + 8 * fq) * 2;
;         const bf16x8 ahi = *(LAS const bf16x8*)(L + TH_HHI + off), alo = *(LAS const bf16x8*)(L + TH_HLO + off);
;         const bf16x8 bhi = *(LAS const bf16x8*)(L + TH_THI + off), blo = *(LAS const bf16x8*)(L + TH_TLO + off);
;         acc = __builtin_amdgcn_mfma_f32_16x16x32_bf16(ahi, bhi, acc, 0, 0, 0);
;         acc = __builtin_amdgcn_mfma_f32_16x16x32_bf16(ahi, blo, acc, 0, 0, 0);
;         acc = __builtin_amdgcn_mfma_f32_16x16x32_bf16(alo, bhi, acc, 0, 0, 0); }
;     LAS float* P = (LAS float*)(L + TH_PART) + wave * 256;
; #pragma unroll
;     for (int t2 = 0; t2 < 4; ++t2) P[(4 * fq + t2) * 16 + fr] = acc[t2];
; }
; __device__ __forceinline__ void p7_norm2(const Frame& F, int layer) {
;     ...
;         thin_mfma_partial(F.lds, F.wave, lane);
;         lds_barrier();
;         if (F.wave < 4) { const int t16 = F.wave * 64 + lane, srow = t16 >> 4, c = t16 & 15; const float lg = thin_total(F.lds, t16);
;             float mx = lg;
; #pragma unroll
;             for (int o = 1; o < 16; o <<= 1) mx = fmaxf(mx, shx(mx, o, lane));
;             const float ex = __expf(lg - mx); float se = ex;
; #pragma unroll
;             for (int o = 1; o < 16; o <<= 1) se += shx(se, o, lane);
;             const int row = (F.blk * NWAVES + (srow >> 1)) * RW + 2 * pi + (srow & 1);
;             if (row < nrows) { const float a = ex / se;
;                 if (row < NL) AFFp[((size_t)((row >> 11) * 16 + c)) * 2048 + (row & 2047)] = a;
;                 else { const int r = row - NL; AFFp[(size_t)NL * 16 + ((size_t)((r >> 8) * 16 + c)) * 256 + (r & 255)] = a; } } }
	v_add_u32_e32 v90, 0x10200, v106
	ds_read_b128 v[62:65], v90
	ds_read_b128 v[66:69], v106
	ds_read_b128 v[70:73], v90 offset:64
	ds_read_b128 v[74:77], v106 offset:64
	ds_read_b128 v[82:85], v106 offset:33024
	ds_read_b128 v[86:89], v106 offset:33088
	s_waitcnt lgkmcnt(4)
	v_mfma_f32_16x16x32_bf16 v[78:81], v[62:65], v[66:69], 0
	v_add_u32_e32 v91, 0x18300, v106
	s_andn2_b64 vcc, exec, s[6:7]
	s_waitcnt lgkmcnt(1)
	v_mfma_f32_16x16x32_bf16 v[62:65], v[62:65], v[82:85], v[78:81]
	s_nop 3
	ds_read_b128 v[78:81], v91
	ds_read_b128 v[82:85], v91 offset:64
	s_waitcnt lgkmcnt(1)
	v_mfma_f32_16x16x32_bf16 v[62:65], v[78:81], v[66:69], v[62:65]
	ds_read_b128 v[66:69], v90 offset:128
	v_mfma_f32_16x16x32_bf16 v[62:65], v[70:73], v[74:77], v[62:65]
	v_mfma_f32_16x16x32_bf16 v[62:65], v[70:73], v[86:89], v[62:65]
	s_waitcnt lgkmcnt(1)
	v_mfma_f32_16x16x32_bf16 v[62:65], v[82:85], v[74:77], v[62:65]
	ds_read_b128 v[70:73], v106 offset:128
	ds_read_b128 v[74:77], v90 offset:192
	ds_read_b128 v[78:81], v106 offset:192
	ds_read_b128 v[82:85], v106 offset:33152
	ds_read_b128 v[86:89], v106 offset:33216
	s_waitcnt lgkmcnt(4)
	v_mfma_f32_16x16x32_bf16 v[62:65], v[66:69], v[70:73], v[62:65]
	s_waitcnt lgkmcnt(1)
	v_mfma_f32_16x16x32_bf16 v[62:65], v[66:69], v[82:85], v[62:65]
	ds_read_b128 v[66:69], v91 offset:128
	ds_read_b128 v[82:85], v91 offset:192
	s_waitcnt lgkmcnt(1)
	v_mfma_f32_16x16x32_bf16 v[62:65], v[66:69], v[70:73], v[62:65]
	v_mfma_f32_16x16x32_bf16 v[62:65], v[74:77], v[78:81], v[62:65]
	v_mfma_f32_16x16x32_bf16 v[62:65], v[74:77], v[86:89], v[62:65]
	s_waitcnt lgkmcnt(0)
	v_mfma_f32_16x16x32_bf16 v[62:65], v[82:85], v[78:81], v[62:65]
	s_nop 7
	ds_write2_b32 v105, v62, v63 offset1:16
	ds_write2_b32 v105, v64, v65 offset0:32 offset1:48
	s_waitcnt vmcnt(0)
	s_waitcnt lgkmcnt(0)
	s_barrier
	s_cbranch_vccnz .LBB0_828
	ds_read2st64_b32 v[62:63], v97 offset1:4
	s_waitcnt lgkmcnt(0)
	v_add_f32_e32 v62, 0, v62
	v_add_f32_e32 v64, v62, v63
	ds_read2st64_b32 v[62:63], v97 offset0:8 offset1:12
	s_waitcnt lgkmcnt(0)
	v_add_f32_e32 v62, v64, v62
	v_add_f32_e32 v64, v62, v63
	ds_read2st64_b32 v[62:63], v97 offset0:16 offset1:20
	s_waitcnt lgkmcnt(0)
	v_add_f32_e32 v62, v64, v62
	v_add_f32_e32 v64, v62, v63
	ds_read2st64_b32 v[62:63], v97 offset0:24 offset1:28
	s_waitcnt lgkmcnt(0)
	v_add_f32_e32 v62, v64, v62
	v_add_f32_e32 v62, v62, v63
	s_nop 1
	v_max_f32_dpp v63, v62, v62 quad_perm:[1,0,3,2] row_mask:0xf bank_mask:0xf
	s_nop 1
	v_max_f32_dpp v63, v63, v63 quad_perm:[2,3,0,1] row_mask:0xf bank_mask:0xf
	s_nop 1
	v_max_f32_dpp v63, v63, v63 row_half_mirror row_mask:0xf bank_mask:0xf
	s_nop 1
	v_max_f32_dpp v63, v63, v63 row_mirror row_mask:0xf bank_mask:0xf
	v_sub_f32_e32 v62, v62, v63
	v_mul_f32_e32 v62, 0x3fb8aa3b, v62
	v_exp_f32_e32 v63, v62
	s_nop 1
	v_add_f32_dpp v62, v63, v63 quad_perm:[1,0,3,2] row_mask:0xf bank_mask:0xf
	s_nop 1
	v_add_f32_dpp v62, v62, v62 quad_perm:[2,3,0,1] row_mask:0xf bank_mask:0xf
	s_nop 1
	v_add_f32_dpp v64, v62, v62 row_half_mirror row_mask:0xf bank_mask:0xf
	s_nop 1
	v_mov_b32_dpp v65, v64 row_mirror row_mask:0xf bank_mask:0xf
	v_add_u32_e32 v62, v96, v102
	v_cmp_gt_i32_e32 vcc, s18, v62
	s_and_saveexec_b64 s[10:11], vcc
	s_cbranch_execz .LBB0_827
	s_waitcnt lgkmcnt(0)
	v_add_f32_e32 v64, v64, v65
	v_div_scale_f32 v65, s[12:13], v64, v64, v63
	v_rcp_f32_e32 v66, v65
	v_div_scale_f32 v67, vcc, v63, v64, v63
	s_movk_i32 s3, 0x7fff
	v_fma_f32 v68, -v65, v66, 1.0
	v_fmac_f32_e32 v66, v68, v66
	v_mul_f32_e32 v68, v67, v66
	v_fma_f32 v69, -v65, v68, v67
	v_fmac_f32_e32 v68, v69, v66
	v_fma_f32 v65, -v65, v68, v67
	v_div_fmas_f32 v65, v65, v66, v68
	v_div_fixup_f32 v63, v65, v64, v63
	v_cmp_lt_i32_e32 vcc, s3, v62
	s_and_saveexec_b64 s[12:13], vcc
	s_xor_b64 s[12:13], exec, s[12:13]
	s_cbranch_execz .LBB0_841
	v_add_u32_e32 v64, 0xffff8000, v102
	v_lshrrev_b32_e32 v64, 4, v64
	s_mov_b32 s3, 0xffffff0
	v_and_or_b32 v144, v64, s3, v95
	v_lshlrev_b64 v[64:65], 10, v[144:145]
	v_mov_b32_e32 v66, 2
	v_lshl_add_u64 v[64:65], s[4:5], 0, v[64:65]
	v_lshlrev_b32_sdwa v144, v66, v62 dst_sel:DWORD dst_unused:UNUSED_PAD src0_sel:DWORD src1_sel:BYTE_0
	v_lshl_add_u64 v[64:65], v[64:65], 0, v[144:145]
	v_add_co_u32_e32 v64, vcc, 0x200000, v64
	s_nop 1
	v_addc_co_u32_e32 v65, vcc, 0, v65, vcc
	global_store_dword v[64:65], v63, off
